# v21 + the first-arriving workgroup of each XCD starts an early L2 write-back after arriving at the grid barrier
# baseline (speedup 1.0000x reference)
.LBB0_92:
	s_or_b64 exec, exec, s[8:9]
	v_cvt_f32_u32_e32 v5, v3
	s_waitcnt vmcnt(0)
	v_readfirstlane_b32 s6, v4
	v_sub_u32_e32 v4, 0, v3
	v_rcp_iflag_f32_e32 v5, v5
	v_add_u32_e32 v6, s6, v2
	v_mul_f32_e32 v5, 0x4f7ffffe, v5
	v_cvt_u32_f32_e32 v5, v5
	v_mul_lo_u32 v2, v4, v5
	v_mul_hi_u32 v2, v5, v2
	v_add_u32_e32 v2, v5, v2
	v_mul_hi_u32 v2, v6, v2
	v_mul_lo_u32 v4, v2, v3
	v_sub_u32_e32 v4, v6, v4
	v_add_u32_e32 v5, 1, v2
	v_cmp_ge_u32_e32 vcc, v4, v3
	s_nop 1
	v_cndmask_b32_e32 v2, v2, v5, vcc
	v_sub_u32_e32 v5, v4, v3
	v_cndmask_b32_e32 v4, v4, v5, vcc
	v_add_u32_e32 v5, 1, v2
	v_cmp_ge_u32_e32 vcc, v4, v3
	v_add_u32_e32 v4, 1, v6
	s_nop 0
	v_cndmask_b32_e32 v2, v2, v5, vcc
	v_mul_lo_u32 v5, v3, v2
	v_add_u32_e32 v3, v5, v3
	v_cmp_ne_u32_e32 vcc, v4, v3
	s_and_saveexec_b64 s[6:7], vcc
	s_xor_b64 s[6:7], exec, s[6:7]
	s_cbranch_execz .LBB0_106
	s_waitcnt lgkmcnt(0)
	v_cmp_eq_u32_e32 vcc, v6, v5
	s_cbranch_vccz .Lbarfl_0
	buffer_wbl2 sc1
.Lbarfl_0:
	v_mov_b32_e32 v1, 0x7100
	global_load_dword v1, v1, s[50:51] offset:1024 sc1
	s_add_u32 s12, s50, 0x7500
	s_addc_u32 s13, s51, 0
	s_waitcnt vmcnt(0)
	v_cmp_eq_u32_e32 vcc, v1, v2
	s_and_saveexec_b64 s[8:9], vcc
	s_cbranch_execz .LBB0_105
	s_add_u32 s10, s50, 0x4200
	s_addc_u32 s11, s51, 0
	s_mov_b32 s24, 1
	s_mov_b64 s[14:15], 0
	v_mov_b32_e32 v1, 0
	s_branch .LBB0_96

.LBB0_2025:
	s_or_b64 exec, exec, s[8:9]
	v_cvt_f32_u32_e32 v4, v2
	s_waitcnt vmcnt(0)
	v_readfirstlane_b32 s6, v3
	v_sub_u32_e32 v3, 0, v2
	v_rcp_iflag_f32_e32 v4, v4
	v_add_u32_e32 v5, s6, v1
	v_mul_f32_e32 v4, 0x4f7ffffe, v4
	v_cvt_u32_f32_e32 v4, v4
	v_mul_lo_u32 v1, v3, v4
	v_mul_hi_u32 v1, v4, v1
	v_add_u32_e32 v1, v4, v1
	v_mul_hi_u32 v1, v5, v1
	v_mul_lo_u32 v3, v1, v2
	v_sub_u32_e32 v3, v5, v3
	v_add_u32_e32 v4, 1, v1
	v_cmp_ge_u32_e32 vcc, v3, v2
	s_nop 1
	v_cndmask_b32_e32 v1, v1, v4, vcc
	v_sub_u32_e32 v4, v3, v2
	v_cndmask_b32_e32 v3, v3, v4, vcc
	v_add_u32_e32 v4, 1, v1
	v_cmp_ge_u32_e32 vcc, v3, v2
	v_add_u32_e32 v3, 1, v5
	s_nop 0
	v_cndmask_b32_e32 v1, v1, v4, vcc
	v_mul_lo_u32 v4, v2, v1
	v_add_u32_e32 v2, v4, v2
	v_cmp_ne_u32_e32 vcc, v3, v2
	s_and_saveexec_b64 s[6:7], vcc
	s_xor_b64 s[6:7], exec, s[6:7]
	s_cbranch_execz .LBB0_2039
	s_waitcnt lgkmcnt(0)
	v_cmp_eq_u32_e32 vcc, v5, v4
	s_cbranch_vccz .Lbarfl_11
	buffer_wbl2 sc1
.Lbarfl_11:
	v_mov_b32_e32 v0, 0x7100
	global_load_dword v0, v0, s[50:51] offset:1024 sc1
	s_add_u32 s12, s50, 0x7500
	s_addc_u32 s13, s51, 0
	s_waitcnt vmcnt(0)
	v_cmp_eq_u32_e32 vcc, v0, v1
	s_and_saveexec_b64 s[8:9], vcc
	s_cbranch_execz .LBB0_2038
	s_add_u32 s10, s50, 0x4200
	s_addc_u32 s11, s51, 0
	s_mov_b32 s24, 1
	s_mov_b64 s[14:15], 0
	v_mov_b32_e32 v0, 0
	s_branch .LBB0_2029
